# attention epilogue RMS-norm butterflies: 80 ds_bpermute hops -> DPP moves / permlane16_swap (on top of v71)
# speedup vs baseline: 1.0262x; 1.0112x over previous
.LBB0_565:
	s_andn2_b64 vcc, exec, s[6:7]
	s_waitcnt lgkmcnt(0)
	s_barrier
	s_cbranch_vccnz .LBB0_409
	v_add_u32_e32 v40, s10, v2
	v_or_b32_e32 v128, 1, v224
	v_lshl_add_u32 v129, v221, 11, v40
	v_lshl_add_u32 v146, v128, 9, v40
	v_or_b32_e32 v127, 2, v224
	v_or_b32_e32 v126, 3, v224
	v_or_b32_e32 v125, 8, v224
	v_or_b32_e32 v124, 9, v224
	v_or_b32_e32 v123, 10, v224
	v_or_b32_e32 v122, 11, v224
	v_or_b32_e32 v119, 18, v224
	v_or_b32_e32 v117, 24, v224
	v_or_b32_e32 v116, 25, v224
	v_or_b32_e32 v115, 26, v224
	v_or_b32_e32 v114, 27, v224
	ds_read2_b32 v[24:25], v129 offset1:32
	ds_read2_b32 v[28:29], v146 offset1:32
	v_lshl_add_u32 v147, v127, 9, v40
	v_lshl_add_u32 v148, v126, 9, v40
	v_lshl_add_u32 v149, v125, 9, v40
	v_lshl_add_u32 v150, v124, 9, v40
	v_lshl_add_u32 v151, v123, 9, v40
	v_lshl_add_u32 v152, v122, 9, v40
	v_lshl_add_u32 v155, v119, 9, v40
	v_lshl_add_u32 v157, v117, 9, v40
	v_lshl_add_u32 v158, v116, 9, v40
	v_lshl_add_u32 v159, v115, 9, v40
	v_lshl_add_u32 v160, v114, 9, v40
	ds_read2_b32 v[32:33], v147 offset1:32
	ds_read2_b32 v[36:37], v148 offset1:32
	ds_read2_b32 v[42:43], v149 offset1:32
	ds_read2_b32 v[44:45], v150 offset1:32
	ds_read2_b32 v[48:49], v151 offset1:32
	ds_read2_b32 v[58:59], v152 offset1:32
	v_or_b32_e32 v121, 16, v224
	ds_read2_b32 v[64:65], v155 offset1:32
	ds_read2_b32 v[130:131], v157 offset1:32
	ds_read2_b32 v[132:133], v158 offset1:32
	ds_read2_b32 v[134:135], v159 offset1:32
	ds_read2_b32 v[136:137], v160 offset1:32
	v_lshl_add_u32 v153, v121, 9, v40
	ds_read2_b32 v[60:61], v153 offset1:32
	v_or_b32_e32 v120, 17, v224
	v_or_b32_e32 v118, 19, v224
	v_lshl_add_u32 v154, v120, 9, v40
	v_lshl_add_u32 v156, v118, 9, v40
	s_waitcnt lgkmcnt(13)
	v_pk_fma_f32 v[56:57], v[198:199], v[24:25], v[4:5] neg_lo:[1,0,0] neg_hi:[1,0,0]
	s_waitcnt lgkmcnt(12)
	v_pk_fma_f32 v[52:53], v[198:199], v[28:29], v[6:7] neg_lo:[1,0,0] neg_hi:[1,0,0]
	ds_read2_b32 v[62:63], v154 offset1:32
	ds_read2_b32 v[82:83], v156 offset1:32
	v_pk_mul_f32 v[138:139], v[56:57], v[56:57]
	v_pk_mul_f32 v[140:141], v[52:53], v[52:53]
	s_waitcnt lgkmcnt(13)
	v_pk_fma_f32 v[46:47], v[198:199], v[32:33], v[8:9] neg_lo:[1,0,0] neg_hi:[1,0,0]
	s_waitcnt lgkmcnt(12)
	v_pk_fma_f32 v[40:41], v[198:199], v[36:37], v[10:11] neg_lo:[1,0,0] neg_hi:[1,0,0]
	s_waitcnt lgkmcnt(11)
	v_pk_fma_f32 v[36:37], v[198:199], v[42:43], v[12:13] neg_lo:[1,0,0] neg_hi:[1,0,0]
	s_waitcnt lgkmcnt(10)
	v_pk_fma_f32 v[32:33], v[198:199], v[44:45], v[14:15] neg_lo:[1,0,0] neg_hi:[1,0,0]
	s_waitcnt lgkmcnt(9)
	v_pk_fma_f32 v[28:29], v[198:199], v[48:49], v[16:17] neg_lo:[1,0,0] neg_hi:[1,0,0]
	s_waitcnt lgkmcnt(8)
	v_pk_fma_f32 v[24:25], v[198:199], v[58:59], v[20:21] neg_lo:[1,0,0] neg_hi:[1,0,0]
	s_waitcnt lgkmcnt(7)
	v_pk_fma_f32 v[14:15], v[198:199], v[64:65], v[72:73] neg_lo:[1,0,0] neg_hi:[1,0,0]
	s_waitcnt lgkmcnt(6)
	v_pk_fma_f32 v[10:11], v[198:199], v[130:131], v[106:107] neg_lo:[1,0,0] neg_hi:[1,0,0]
	s_waitcnt lgkmcnt(5)
	v_pk_fma_f32 v[8:9], v[198:199], v[132:133], v[108:109] neg_lo:[1,0,0] neg_hi:[1,0,0]
	s_waitcnt lgkmcnt(4)
	v_pk_fma_f32 v[6:7], v[198:199], v[134:135], v[110:111] neg_lo:[1,0,0] neg_hi:[1,0,0]
	s_waitcnt lgkmcnt(3)
	v_pk_fma_f32 v[4:5], v[198:199], v[136:137], v[112:113] neg_lo:[1,0,0] neg_hi:[1,0,0]
	ds_read2_b32 v[42:43], v129 offset0:64 offset1:96
	ds_read2_b32 v[44:45], v146 offset0:64 offset1:96
	ds_read2_b32 v[48:49], v147 offset0:64 offset1:96
	ds_read2_b32 v[58:59], v148 offset0:64 offset1:96
	ds_read2_b32 v[106:107], v149 offset0:64 offset1:96
	ds_read2_b32 v[108:109], v150 offset0:64 offset1:96
	ds_read2_b32 v[110:111], v151 offset0:64 offset1:96
	ds_read2_b32 v[112:113], v152 offset0:64 offset1:96
	ds_read2_b32 v[130:131], v153 offset0:64 offset1:96
	ds_read2_b32 v[132:133], v154 offset0:64 offset1:96
	ds_read2_b32 v[134:135], v155 offset0:64 offset1:96
	ds_read2_b32 v[136:137], v156 offset0:64 offset1:96
	ds_read2_b32 v[146:147], v157 offset0:64 offset1:96
	ds_read2_b32 v[148:149], v158 offset0:64 offset1:96
	ds_read2_b32 v[150:151], v159 offset0:64 offset1:96
	ds_read2_b32 v[152:153], v160 offset0:64 offset1:96
	s_waitcnt lgkmcnt(14)
	v_pk_fma_f32 v[66:67], v[198:199], v[42:43], v[66:67] neg_lo:[1,0,0] neg_hi:[1,0,0]
	v_pk_fma_f32 v[64:65], v[198:199], v[44:45], v[50:51] neg_lo:[1,0,0] neg_hi:[1,0,0]
	v_pk_mul_f32 v[154:155], v[66:67], v[66:67]
	v_pk_mul_f32 v[44:45], v[64:65], v[64:65]
	v_mov_b32_e32 v50, v140
	v_mov_b32_e32 v51, v138
	v_mov_b32_e32 v138, v141
	v_pk_fma_f32 v[20:21], v[198:199], v[60:61], v[68:69] neg_lo:[1,0,0] neg_hi:[1,0,0]
	s_waitcnt lgkmcnt(12)
	v_pk_fma_f32 v[60:61], v[198:199], v[58:59], v[90:91] neg_lo:[1,0,0] neg_hi:[1,0,0]
	v_pk_add_f32 v[50:51], v[50:51], v[138:139]
	v_mov_b32_e32 v90, v44
	v_mov_b32_e32 v91, v154
	v_pk_add_f32 v[50:51], v[50:51], v[90:91]
	v_mov_b32_e32 v154, v45
	v_pk_add_f32 v[90:91], v[50:51], v[154:155]
	s_waitcnt lgkmcnt(11)
	v_pk_fma_f32 v[58:59], v[198:199], v[106:107], v[92:93] neg_lo:[1,0,0] neg_hi:[1,0,0]
	v_mov_b32_e32 v93, v91
	s_nop 1
	v_permlane16_swap_b32_e32 v93, v91
	v_mov_b32_e32 v92, v90
	s_nop 1
	v_permlane16_swap_b32_e32 v92, v90
	s_waitcnt lgkmcnt(7)
	v_pk_fma_f32 v[50:51], v[198:199], v[130:131], v[30:31] neg_lo:[1,0,0] neg_hi:[1,0,0]
	v_pk_fma_f32 v[42:43], v[198:199], v[112:113], v[100:101] neg_lo:[1,0,0] neg_hi:[1,0,0]
	v_pk_mul_f32 v[142:143], v[46:47], v[46:47]
	v_pk_mul_f32 v[144:145], v[40:41], v[40:41]
	s_waitcnt lgkmcnt(0)
	v_pk_add_f32 v[30:31], v[90:91], v[92:93]
	s_nop 1
	v_mov_b32_dpp v91, v31 row_ror:8 row_mask:0xf bank_mask:0xf
	s_nop 1
	v_mov_b32_dpp v90, v30 row_ror:8 row_mask:0xf bank_mask:0xf
	v_pk_fma_f32 v[16:17], v[198:199], v[62:63], v[70:71] neg_lo:[1,0,0] neg_hi:[1,0,0]
	v_pk_fma_f32 v[62:63], v[198:199], v[48:49], v[84:85] neg_lo:[1,0,0] neg_hi:[1,0,0]
	v_pk_mul_f32 v[156:157], v[60:61], v[60:61]
	v_pk_mul_f32 v[84:85], v[62:63], v[62:63]
	s_waitcnt lgkmcnt(0)
	v_pk_add_f32 v[92:93], v[30:31], v[90:91]
	s_nop 1
	v_mov_b32_dpp v113, v93 row_shr:4 row_mask:0xf bank_mask:0xa
	v_mov_b32_dpp v113, v93 row_shl:4 row_mask:0xf bank_mask:0x5
	s_nop 1
	v_mov_b32_dpp v112, v92 row_shr:4 row_mask:0xf bank_mask:0xa
	v_mov_b32_dpp v112, v92 row_shl:4 row_mask:0xf bank_mask:0x5
	v_pk_fma_f32 v[30:31], v[198:199], v[146:147], v[22:23] neg_lo:[1,0,0] neg_hi:[1,0,0]
	v_pk_fma_f32 v[22:23], v[198:199], v[150:151], v[18:19] neg_lo:[1,0,0] neg_hi:[1,0,0]
	v_pk_fma_f32 v[18:19], v[198:199], v[152:153], v[78:79] neg_lo:[1,0,0] neg_hi:[1,0,0]
	v_pk_fma_f32 v[44:45], v[198:199], v[132:133], v[38:39] neg_lo:[1,0,0] neg_hi:[1,0,0]
	s_waitcnt lgkmcnt(0)
	v_pk_add_f32 v[112:113], v[92:93], v[112:113]
	s_nop 1
	v_mov_b32_dpp v131, v113 quad_perm:[2,3,0,1] row_mask:0xf bank_mask:0xf
	s_nop 1
	v_mov_b32_dpp v130, v112 quad_perm:[2,3,0,1] row_mask:0xf bank_mask:0xf
	v_mov_b32_e32 v132, v156
	v_mov_b32_e32 v133, v84
	v_mov_b32_e32 v84, v157
	v_pk_mul_f32 v[102:103], v[36:37], v[36:37]
	s_waitcnt lgkmcnt(0)
	v_pk_add_f32 v[78:79], v[112:113], v[130:131]
	v_mov_b32_e32 v130, v144
	v_mov_b32_e32 v131, v142
	v_mov_b32_e32 v142, v145
	v_pk_add_f32 v[130:131], v[130:131], v[142:143]
	v_pk_mul_f32 v[104:105], v[32:33], v[32:33]
	v_pk_add_f32 v[130:131], v[130:131], v[132:133]
	v_pk_fma_f32 v[54:55], v[198:199], v[108:109], v[54:55] neg_lo:[1,0,0] neg_hi:[1,0,0]
	v_pk_add_f32 v[130:131], v[130:131], v[84:85]
	v_mov_b32_e32 v133, v131
	s_nop 1
	v_permlane16_swap_b32_e32 v133, v131
	v_mov_b32_e32 v132, v130
	s_nop 1
	v_permlane16_swap_b32_e32 v132, v130
	v_pk_mul_f32 v[158:159], v[58:59], v[58:59]
	v_pk_mul_f32 v[160:161], v[54:55], v[54:55]
	v_pk_fma_f32 v[38:39], v[198:199], v[134:135], v[26:27] neg_lo:[1,0,0] neg_hi:[1,0,0]
	v_mov_b32_e32 v134, v104
	s_waitcnt lgkmcnt(0)
	v_pk_add_f32 v[130:131], v[130:131], v[132:133]
	s_nop 1
	v_mov_b32_dpp v133, v131 row_ror:8 row_mask:0xf bank_mask:0xf
	s_nop 1
	v_mov_b32_dpp v132, v130 row_ror:8 row_mask:0xf bank_mask:0xf
	v_mov_b32_e32 v135, v102
	v_mov_b32_e32 v102, v105
	v_pk_add_f32 v[102:103], v[134:135], v[102:103]
	v_mov_b32_e32 v104, v160
	s_waitcnt lgkmcnt(0)
	v_pk_add_f32 v[130:131], v[130:131], v[132:133]
	s_nop 1
	v_mov_b32_dpp v133, v131 row_shr:4 row_mask:0xf bank_mask:0xa
	v_mov_b32_dpp v133, v131 row_shl:4 row_mask:0xf bank_mask:0x5
	s_nop 1
	v_mov_b32_dpp v132, v130 row_shr:4 row_mask:0xf bank_mask:0xa
	v_mov_b32_dpp v132, v130 row_shl:4 row_mask:0xf bank_mask:0x5
	v_mov_b32_e32 v105, v158
	v_pk_add_f32 v[102:103], v[102:103], v[104:105]
	v_mov_b32_e32 v158, v161
	v_pk_add_f32 v[104:105], v[102:103], v[158:159]
	s_waitcnt lgkmcnt(0)
	v_pk_add_f32 v[130:131], v[130:131], v[132:133]
	s_nop 1
	v_mov_b32_dpp v133, v131 quad_perm:[2,3,0,1] row_mask:0xf bank_mask:0xf
	s_nop 1
	v_mov_b32_dpp v132, v130 quad_perm:[2,3,0,1] row_mask:0xf bank_mask:0xf
	v_mov_b32_e32 v135, v105
	s_nop 1
	v_permlane16_swap_b32_e32 v135, v105
	v_mov_b32_e32 v134, v104
	s_nop 1
	v_permlane16_swap_b32_e32 v134, v104
	s_lshl_b64 s[6:7], s[86:87], 12
	s_nop 1
	v_mov_b32_dpp v113, v79 quad_perm:[1,0,3,2] row_mask:0xf bank_mask:0xf
	s_waitcnt lgkmcnt(3)
	v_pk_add_f32 v[130:131], v[130:131], v[132:133]
	s_nop 1
	v_mov_b32_dpp v133, v131 quad_perm:[1,0,3,2] row_mask:0xf bank_mask:0xf
	s_nop 1
	v_mov_b32_dpp v132, v130 quad_perm:[1,0,3,2] row_mask:0xf bank_mask:0xf
	s_waitcnt lgkmcnt(3)
	v_pk_add_f32 v[104:105], v[104:105], v[134:135]
	s_nop 1
	v_mov_b32_dpp v112, v78 quad_perm:[1,0,3,2] row_mask:0xf bank_mask:0xf
	s_add_u32 s1, s26, s6
	s_addc_u32 s6, s27, s7
	s_waitcnt lgkmcnt(1)
	v_pk_add_f32 v[130:131], v[130:131], v[132:133]
	s_nop 1
	v_mov_b32_dpp v133, v105 row_ror:8 row_mask:0xf bank_mask:0xf
	s_nop 1
	v_mov_b32_dpp v132, v104 row_ror:8 row_mask:0xf bank_mask:0xf
	s_add_u32 s8, s1, s88
	s_addc_u32 s9, s6, s89
	s_mov_b32 s6, 0x3727c5ac
	s_waitcnt lgkmcnt(2)
	v_pk_add_f32 v[112:113], v[78:79], v[112:113]
	s_waitcnt lgkmcnt(0)
	v_pk_add_f32 v[104:105], v[104:105], v[132:133]
	s_nop 1
	v_mov_b32_dpp v133, v105 row_shr:4 row_mask:0xf bank_mask:0xa
	v_mov_b32_dpp v133, v105 row_shl:4 row_mask:0xf bank_mask:0x5
	s_nop 1
	v_mov_b32_dpp v132, v104 row_shr:4 row_mask:0xf bank_mask:0xa
	v_mov_b32_dpp v132, v104 row_shl:4 row_mask:0xf bank_mask:0x5
	v_mov_b64_e32 v[78:79], s[6:7]
	s_brev_b32 s10, 60
	v_pk_mul_f32 v[94:95], v[28:29], v[28:29]
	v_pk_mul_f32 v[96:97], v[24:25], v[24:25]
	v_pk_fma_f32 v[48:49], v[198:199], v[110:111], v[98:99] neg_lo:[1,0,0] neg_hi:[1,0,0]
	v_pk_fma_f32 v[112:113], v[112:113], s[10:11], v[78:79] op_sel_hi:[1,0,0]
	s_mov_b32 s1, 0x800000
	v_pk_mul_f32 v[110:111], v[48:49], v[48:49]
	v_pk_mul_f32 v[138:139], v[42:43], v[42:43]
	v_mul_f32_e32 v129, 0x4b800000, v113
	v_cmp_gt_f32_e32 vcc, s1, v113
	s_waitcnt lgkmcnt(0)
	v_pk_add_f32 v[104:105], v[104:105], v[132:133]
	v_mov_b32_e32 v132, v96
	v_mov_b32_e32 v133, v94
	v_mov_b32_e32 v94, v97
	v_cndmask_b32_e32 v113, v113, v129, vcc
	v_mul_f32_e32 v129, 0x4b800000, v112
	v_cmp_gt_f32_e64 s[6:7], s1, v112
	v_pk_add_f32 v[94:95], v[132:133], v[94:95]
	v_mov_b32_e32 v96, v138
	v_mov_b32_e32 v97, v110
	v_rsq_f32_e32 v113, v113
	v_cndmask_b32_e64 v112, v112, v129, s[6:7]
	v_pk_add_f32 v[94:95], v[94:95], v[96:97]
	v_mov_b32_e32 v110, v139
	v_rsq_f32_e32 v129, v112
	v_pk_add_f32 v[94:95], v[94:95], v[110:111]
	v_mov_b32_e32 v97, v95
	s_nop 1
	v_permlane16_swap_b32_e32 v97, v95
	v_mov_b32_e32 v96, v94
	s_nop 1
	v_permlane16_swap_b32_e32 v96, v94
	v_mul_f32_e32 v112, 0x45800000, v113
	v_cndmask_b32_e32 v112, v113, v112, vcc
	v_mul_f32_e32 v113, 0x45800000, v129
	v_pk_fma_f32 v[130:131], v[130:131], s[10:11], v[78:79] op_sel_hi:[1,0,0]
	v_cndmask_b32_e64 v102, v129, v113, s[6:7]
	v_mul_f32_e32 v103, 0x4b800000, v131
	v_cmp_gt_f32_e32 vcc, s1, v131
	v_mul_f32_e32 v113, 0x4b800000, v130
	v_cmp_gt_f32_e64 s[6:7], s1, v130
	v_cndmask_b32_e32 v103, v131, v103, vcc
	s_nop 1
	v_mov_b32_dpp v131, v105 quad_perm:[2,3,0,1] row_mask:0xf bank_mask:0xf
	v_cndmask_b32_e64 v113, v130, v113, s[6:7]
	s_nop 1
	v_mov_b32_dpp v130, v104 quad_perm:[2,3,0,1] row_mask:0xf bank_mask:0xf
	s_waitcnt lgkmcnt(2)
	v_pk_add_f32 v[94:95], v[94:95], v[96:97]
	s_nop 1
	v_mov_b32_dpp v97, v95 row_ror:8 row_mask:0xf bank_mask:0xf
	s_nop 1
	v_mov_b32_dpp v96, v94 row_ror:8 row_mask:0xf bank_mask:0xf
	v_rsq_f32_e32 v103, v103
	s_waitcnt lgkmcnt(2)
	v_pk_add_f32 v[104:105], v[104:105], v[130:131]
	s_nop 1
	v_mov_b32_dpp v131, v105 quad_perm:[1,0,3,2] row_mask:0xf bank_mask:0xf
	s_nop 1
	v_mov_b32_dpp v130, v104 quad_perm:[1,0,3,2] row_mask:0xf bank_mask:0xf
	s_waitcnt lgkmcnt(2)
	v_pk_add_f32 v[94:95], v[94:95], v[96:97]
	s_nop 1
	v_mov_b32_dpp v97, v95 row_shr:4 row_mask:0xf bank_mask:0xa
	v_mov_b32_dpp v97, v95 row_shl:4 row_mask:0xf bank_mask:0x5
	s_nop 1
	v_mov_b32_dpp v96, v94 row_shr:4 row_mask:0xf bank_mask:0xa
	v_mov_b32_dpp v96, v94 row_shl:4 row_mask:0xf bank_mask:0x5
	v_rsq_f32_e32 v113, v113
	s_waitcnt lgkmcnt(2)
	v_pk_add_f32 v[104:105], v[104:105], v[130:131]
	v_mul_f32_e32 v129, 0x45800000, v103
	v_pk_fma_f32 v[104:105], v[104:105], s[10:11], v[78:79] op_sel_hi:[1,0,0]
	s_waitcnt lgkmcnt(0)
	v_pk_add_f32 v[94:95], v[94:95], v[96:97]
	v_cndmask_b32_e32 v103, v103, v129, vcc
	v_mul_f32_e32 v111, 0x4b800000, v105
	v_cmp_gt_f32_e32 vcc, s1, v105
	s_nop 1
	v_mov_b32_dpp v97, v95 quad_perm:[2,3,0,1] row_mask:0xf bank_mask:0xf
	s_nop 1
	v_mov_b32_dpp v96, v94 quad_perm:[2,3,0,1] row_mask:0xf bank_mask:0xf
	v_cndmask_b32_e32 v105, v105, v111, vcc
	v_rsq_f32_e32 v105, v105
	v_mul_f32_e32 v129, 0x45800000, v113
	v_cndmask_b32_e64 v110, v113, v129, s[6:7]
	v_mul_f32_e32 v111, 0x4b800000, v104
	v_cmp_gt_f32_e64 s[6:7], s1, v104
	s_waitcnt lgkmcnt(0)
	v_pk_add_f32 v[94:95], v[94:95], v[96:97]
	s_nop 1
	v_mov_b32_dpp v97, v95 quad_perm:[1,0,3,2] row_mask:0xf bank_mask:0xf
	v_cndmask_b32_e64 v104, v104, v111, s[6:7]
	v_rsq_f32_e32 v111, v104
	v_mul_f32_e32 v104, 0x45800000, v105
	s_nop 1
	v_mov_b32_dpp v96, v94 quad_perm:[1,0,3,2] row_mask:0xf bank_mask:0xf
	v_pk_mul_f32 v[86:87], v[20:21], v[20:21]
	v_pk_mul_f32 v[88:89], v[16:17], v[16:17]
	v_cndmask_b32_e32 v104, v105, v104, vcc
	v_pk_mul_f32 v[106:107], v[50:51], v[50:51]
	v_pk_mul_f32 v[108:109], v[44:45], v[44:45]
	v_mul_f32_e32 v113, 0x3f4ccccd, v104
	v_mov_b32_e32 v104, v88
	v_mov_b32_e32 v105, v86
	v_mov_b32_e32 v86, v89
	v_pk_add_f32 v[86:87], v[104:105], v[86:87]
	v_mov_b32_e32 v88, v108
	v_mov_b32_e32 v89, v106
	v_pk_add_f32 v[86:87], v[86:87], v[88:89]
	v_mov_b32_e32 v106, v109
	v_pk_add_f32 v[86:87], v[86:87], v[106:107]
	s_waitcnt lgkmcnt(0)
	v_pk_add_f32 v[94:95], v[94:95], v[96:97]
	v_mov_b32_e32 v89, v87
	s_nop 1
	v_permlane16_swap_b32_e32 v89, v87
	v_mov_b32_e32 v88, v86
	s_nop 1
	v_permlane16_swap_b32_e32 v88, v86
	v_pk_fma_f32 v[94:95], v[94:95], s[10:11], v[78:79] op_sel_hi:[1,0,0]
	v_mul_f32_e32 v129, 0x45800000, v111
	v_mul_f32_e32 v96, 0x4b800000, v95
	v_cmp_gt_f32_e32 vcc, s1, v95
	v_cndmask_b32_e64 v104, v111, v129, s[6:7]
	s_waitcnt lgkmcnt(0)
	v_pk_add_f32 v[86:87], v[86:87], v[88:89]
	v_cndmask_b32_e32 v95, v95, v96, vcc
	v_rsq_f32_e32 v95, v95
	v_mul_f32_e32 v96, 0x4b800000, v94
	v_cmp_gt_f32_e64 s[6:7], s1, v94
	s_nop 1
	v_mov_b32_dpp v89, v87 row_ror:8 row_mask:0xf bank_mask:0xf
	s_nop 1
	v_mov_b32_dpp v88, v86 row_ror:8 row_mask:0xf bank_mask:0xf
	v_cndmask_b32_e64 v94, v94, v96, s[6:7]
	v_pk_fma_f32 v[12:13], v[198:199], v[82:83], v[74:75] neg_lo:[1,0,0] neg_hi:[1,0,0]
	v_rsq_f32_e32 v96, v94
	v_mul_f32_e32 v94, 0x45800000, v95
	v_pk_mul_f32 v[80:81], v[14:15], v[14:15]
	v_pk_mul_f32 v[82:83], v[12:13], v[12:13]
	v_pk_fma_f32 v[34:35], v[198:199], v[136:137], v[34:35] neg_lo:[1,0,0] neg_hi:[1,0,0]
	v_cndmask_b32_e32 v94, v95, v94, vcc
	v_pk_mul_f32 v[98:99], v[38:39], v[38:39]
	v_pk_mul_f32 v[100:101], v[34:35], v[34:35]
	v_mul_f32_e32 v97, 0x3f4ccccd, v94
	v_mov_b32_e32 v94, v82
	v_mov_b32_e32 v95, v80
	v_mov_b32_e32 v80, v83
	v_pk_add_f32 v[80:81], v[94:95], v[80:81]
	v_mov_b32_e32 v82, v100
	v_mov_b32_e32 v83, v98
	s_waitcnt lgkmcnt(0)
	v_pk_add_f32 v[86:87], v[86:87], v[88:89]
	v_pk_add_f32 v[80:81], v[80:81], v[82:83]
	v_mov_b32_e32 v98, v101
	s_nop 1
	v_mov_b32_dpp v89, v87 row_shr:4 row_mask:0xf bank_mask:0xa
	v_mov_b32_dpp v89, v87 row_shl:4 row_mask:0xf bank_mask:0x5
	s_nop 1
	v_mov_b32_dpp v88, v86 row_shr:4 row_mask:0xf bank_mask:0xa
	v_mov_b32_dpp v88, v86 row_shl:4 row_mask:0xf bank_mask:0x5
	v_pk_add_f32 v[80:81], v[80:81], v[98:99]
	v_mov_b32_e32 v83, v81
	s_nop 1
	v_permlane16_swap_b32_e32 v83, v81
	v_mov_b32_e32 v82, v80
	s_nop 1
	v_permlane16_swap_b32_e32 v82, v80
	v_mul_f32_e32 v105, 0x45800000, v96
	s_waitcnt lgkmcnt(2)
	v_pk_add_f32 v[86:87], v[86:87], v[88:89]
	s_nop 1
	v_mov_b32_dpp v89, v87 quad_perm:[2,3,0,1] row_mask:0xf bank_mask:0xf
	s_nop 1
	v_mov_b32_dpp v88, v86 quad_perm:[2,3,0,1] row_mask:0xf bank_mask:0xf
	s_waitcnt lgkmcnt(2)
	v_pk_add_f32 v[80:81], v[80:81], v[82:83]
	s_nop 1
	v_mov_b32_dpp v83, v81 row_ror:8 row_mask:0xf bank_mask:0xf
	s_nop 1
	v_mov_b32_dpp v82, v80 row_ror:8 row_mask:0xf bank_mask:0xf
	v_cndmask_b32_e64 v94, v96, v105, s[6:7]
	s_waitcnt lgkmcnt(2)
	v_pk_add_f32 v[86:87], v[86:87], v[88:89]
	s_nop 1
	v_mov_b32_dpp v89, v87 quad_perm:[1,0,3,2] row_mask:0xf bank_mask:0xf
	s_nop 1
	v_mov_b32_dpp v88, v86 quad_perm:[1,0,3,2] row_mask:0xf bank_mask:0xf
	s_waitcnt lgkmcnt(2)
	v_pk_add_f32 v[80:81], v[80:81], v[82:83]
	s_nop 1
	v_mov_b32_dpp v83, v81 row_shr:4 row_mask:0xf bank_mask:0xa
	v_mov_b32_dpp v83, v81 row_shl:4 row_mask:0xf bank_mask:0x5
	s_nop 1
	v_mov_b32_dpp v82, v80 row_shr:4 row_mask:0xf bank_mask:0xa
	v_mov_b32_dpp v82, v80 row_shl:4 row_mask:0xf bank_mask:0x5
	v_pk_mul_f32 v[72:73], v[10:11], v[10:11]
	s_waitcnt lgkmcnt(2)
	v_pk_add_f32 v[86:87], v[86:87], v[88:89]
	v_pk_mul_f32 v[74:75], v[8:9], v[8:9]
	v_pk_fma_f32 v[86:87], v[86:87], s[10:11], v[78:79] op_sel_hi:[1,0,0]
	s_waitcnt lgkmcnt(0)
	v_pk_add_f32 v[80:81], v[80:81], v[82:83]
	v_mul_f32_e32 v88, 0x4b800000, v87
	v_cmp_gt_f32_e32 vcc, s1, v87
	s_nop 1
	v_mov_b32_dpp v83, v81 quad_perm:[2,3,0,1] row_mask:0xf bank_mask:0xf
	s_nop 1
	v_mov_b32_dpp v82, v80 quad_perm:[2,3,0,1] row_mask:0xf bank_mask:0xf
	v_cndmask_b32_e32 v87, v87, v88, vcc
	v_rsq_f32_e32 v87, v87
	v_mul_f32_e32 v88, 0x4b800000, v86
	v_cmp_gt_f32_e64 s[6:7], s1, v86
	s_waitcnt lgkmcnt(0)
	v_pk_add_f32 v[80:81], v[80:81], v[82:83]
	s_nop 1
	v_mov_b32_dpp v83, v81 quad_perm:[1,0,3,2] row_mask:0xf bank_mask:0xf
	v_cndmask_b32_e64 v86, v86, v88, s[6:7]
	v_rsq_f32_e32 v88, v86
	v_mul_f32_e32 v86, 0x45800000, v87
	s_nop 1
	v_mov_b32_dpp v82, v80 quad_perm:[1,0,3,2] row_mask:0xf bank_mask:0xf
	v_cndmask_b32_e32 v86, v87, v86, vcc
	v_mul_f32_e32 v89, 0x3f4ccccd, v86
	v_mul_f32_e32 v95, 0x45800000, v88
	v_mov_b32_e32 v86, v74
	v_mov_b32_e32 v87, v72
	v_mov_b32_e32 v72, v75
	v_pk_add_f32 v[72:73], v[86:87], v[72:73]
	v_cndmask_b32_e64 v86, v88, v95, s[6:7]
	v_readlane_b32 s6, v255, 7
	v_readlane_b32 s7, v255, 8
	s_waitcnt lgkmcnt(0)
	v_pk_add_f32 v[80:81], v[80:81], v[82:83]
	v_pk_fma_f32 v[26:27], v[198:199], v[148:149], v[76:77] neg_lo:[1,0,0] neg_hi:[1,0,0]
	v_pk_mul_f32 v[90:91], v[30:31], v[30:31]
	v_pk_mul_f32 v[92:93], v[26:27], v[26:27]
	v_mov_b32_e32 v75, v90
	global_load_dword v83, v2, s[6:7]
	global_load_dword v87, v2, s[6:7] offset:128
	v_mov_b32_e32 v74, v92
	v_pk_add_f32 v[72:73], v[72:73], v[74:75]
	v_mov_b32_e32 v90, v93
	v_pk_add_f32 v[72:73], v[72:73], v[90:91]
	global_load_dword v90, v2, s[6:7] offset:256
	global_load_dword v91, v2, s[6:7] offset:384
	v_mov_b32_e32 v75, v73
	s_nop 1
	v_permlane16_swap_b32_e32 v75, v73
	v_mov_b32_e32 v74, v72
	s_nop 1
	v_permlane16_swap_b32_e32 v74, v72
	v_pk_fma_f32 v[80:81], v[80:81], s[10:11], v[78:79] op_sel_hi:[1,0,0]
	v_pk_mul_f32 v[68:69], v[6:7], v[6:7]
	v_mul_f32_e32 v82, 0x4b800000, v81
	v_cmp_gt_f32_e32 vcc, s1, v81
	s_waitcnt lgkmcnt(0)
	v_pk_add_f32 v[72:73], v[72:73], v[74:75]
	s_nop 1
	v_mov_b32_dpp v75, v73 row_ror:8 row_mask:0xf bank_mask:0xf
	v_cndmask_b32_e32 v81, v81, v82, vcc
	v_rsq_f32_e32 v81, v81
	s_nop 1
	v_mov_b32_dpp v74, v72 row_ror:8 row_mask:0xf bank_mask:0xf
	v_pk_mul_f32 v[70:71], v[4:5], v[4:5]
	v_pk_mul_f32 v[76:77], v[22:23], v[22:23]
	v_mul_f32_e32 v82, 0x45800000, v81
	v_cndmask_b32_e32 v82, v81, v82, vcc
	v_mul_f32_e32 v81, 0x4b800000, v80
	v_cmp_gt_f32_e32 vcc, s1, v80
	v_pk_mul_f32 v[84:85], v[18:19], v[18:19]
	s_waitcnt lgkmcnt(0)
	v_pk_add_f32 v[72:73], v[72:73], v[74:75]
	v_cndmask_b32_e32 v80, v80, v81, vcc
	v_rsq_f32_e32 v88, v80
	v_mov_b32_e32 v80, v70
	v_mov_b32_e32 v81, v68
	v_mov_b32_e32 v68, v71
	s_nop 1
	v_mov_b32_dpp v75, v73 row_shr:4 row_mask:0xf bank_mask:0xa
	v_mov_b32_dpp v75, v73 row_shl:4 row_mask:0xf bank_mask:0x5
	s_nop 1
	v_mov_b32_dpp v74, v72 row_shr:4 row_mask:0xf bank_mask:0xa
	v_mov_b32_dpp v74, v72 row_shl:4 row_mask:0xf bank_mask:0x5
	v_pk_add_f32 v[68:69], v[80:81], v[68:69]
	v_mov_b32_e32 v70, v84
	v_mov_b32_e32 v71, v76
	v_pk_add_f32 v[68:69], v[68:69], v[70:71]
	v_mov_b32_e32 v76, v85
	v_pk_add_f32 v[68:69], v[68:69], v[76:77]
	v_mov_b32_e32 v71, v69
	s_nop 1
	v_permlane16_swap_b32_e32 v71, v69
	v_mov_b32_e32 v70, v68
	s_nop 1
	v_permlane16_swap_b32_e32 v70, v68
	s_waitcnt lgkmcnt(2)
	v_pk_add_f32 v[72:73], v[72:73], v[74:75]
	s_nop 1
	v_mov_b32_dpp v75, v73 quad_perm:[2,3,0,1] row_mask:0xf bank_mask:0xf
	s_nop 1
	v_mov_b32_dpp v74, v72 quad_perm:[2,3,0,1] row_mask:0xf bank_mask:0xf
	v_mul_f32_e32 v2, 0x45800000, v88
	s_waitcnt lgkmcnt(2)
	v_pk_add_f32 v[68:69], v[68:69], v[70:71]
	s_nop 1
	v_mov_b32_dpp v71, v69 row_ror:8 row_mask:0xf bank_mask:0xf
	s_nop 1
	v_mov_b32_dpp v70, v68 row_ror:8 row_mask:0xf bank_mask:0xf
	s_waitcnt lgkmcnt(2)
	v_pk_add_f32 v[72:73], v[72:73], v[74:75]
	s_nop 1
	v_mov_b32_dpp v75, v73 quad_perm:[1,0,3,2] row_mask:0xf bank_mask:0xf
	s_nop 1
	v_mov_b32_dpp v74, v72 quad_perm:[1,0,3,2] row_mask:0xf bank_mask:0xf
	v_cndmask_b32_e32 v2, v88, v2, vcc
	s_waitcnt lgkmcnt(2)
	v_pk_add_f32 v[68:69], v[68:69], v[70:71]
	s_nop 1
	v_mov_b32_dpp v71, v69 row_shr:4 row_mask:0xf bank_mask:0xa
	v_mov_b32_dpp v71, v69 row_shl:4 row_mask:0xf bank_mask:0x5
	s_nop 1
	v_mov_b32_dpp v70, v68 row_shr:4 row_mask:0xf bank_mask:0xa
	v_mov_b32_dpp v70, v68 row_shl:4 row_mask:0xf bank_mask:0x5
	s_waitcnt lgkmcnt(2)
	v_pk_add_f32 v[72:73], v[72:73], v[74:75]
	v_mul_f32_e32 v112, 0x3f4ccccd, v112
	v_pk_fma_f32 v[72:73], v[72:73], s[10:11], v[78:79] op_sel_hi:[1,0,0]
	v_mul_f32_e32 v102, 0x3f4ccccd, v102
	v_mul_f32_e32 v74, 0x4b800000, v73
	v_cmp_gt_f32_e64 s[6:7], s1, v73
	s_waitcnt lgkmcnt(0)
	v_pk_add_f32 v[68:69], v[68:69], v[70:71]
	s_nop 1
	v_mov_b32_dpp v71, v69 quad_perm:[2,3,0,1] row_mask:0xf bank_mask:0xf
	v_cndmask_b32_e64 v73, v73, v74, s[6:7]
	v_rsq_f32_e32 v73, v73
	s_nop 1
	v_mov_b32_dpp v70, v68 quad_perm:[2,3,0,1] row_mask:0xf bank_mask:0xf
	v_mul_f32_e32 v74, 0x3f4ccccd, v2
	v_cmp_gt_f32_e32 vcc, s1, v72
	v_mul_f32_e32 v2, 0x45800000, v73
	v_cndmask_b32_e64 v2, v73, v2, s[6:7]
	v_mul_f32_e32 v73, 0x4b800000, v72
	s_waitcnt lgkmcnt(0)
	v_pk_add_f32 v[68:69], v[68:69], v[70:71]
	v_cndmask_b32_e32 v72, v72, v73, vcc
	s_nop 1
	v_mov_b32_dpp v71, v69 quad_perm:[1,0,3,2] row_mask:0xf bank_mask:0xf
	s_nop 1
	v_mov_b32_dpp v70, v68 quad_perm:[1,0,3,2] row_mask:0xf bank_mask:0xf
	v_rsq_f32_e32 v72, v72
	v_mul_f32_e32 v73, 0x3f4ccccd, v2
	v_mul_f32_e32 v103, 0x3f4ccccd, v103
	v_mul_f32_e32 v110, 0x3f4ccccd, v110
	v_mul_f32_e32 v2, 0x45800000, v72
	s_waitcnt lgkmcnt(0)
	v_pk_add_f32 v[68:69], v[68:69], v[70:71]
	v_cndmask_b32_e32 v2, v72, v2, vcc
	v_pk_fma_f32 v[68:69], v[68:69], s[10:11], v[78:79] op_sel_hi:[1,0,0]
	v_mul_f32_e32 v72, 0x3f4ccccd, v2
	v_mul_f32_e32 v2, 0x4b800000, v69
	v_cmp_gt_f32_e32 vcc, s1, v69
	v_cmp_gt_f32_e64 s[6:7], s1, v68
	v_or_b32_e32 v70, s0, v224
	v_cndmask_b32_e32 v2, v69, v2, vcc
	v_rsq_f32_e32 v2, v2
	v_mul_f32_e32 v69, 0x4b800000, v68
	v_cndmask_b32_e64 v68, v68, v69, s[6:7]
	v_rsq_f32_e32 v68, v68
	v_mul_f32_e32 v69, 0x45800000, v2
	v_cndmask_b32_e32 v2, v2, v69, vcc
	v_mul_f32_e32 v75, 0x3f4ccccd, v2
	v_mul_f32_e32 v2, 0x45800000, v68
	v_cndmask_b32_e64 v2, v68, v2, s[6:7]
	v_mul_f32_e32 v77, 0x3f4ccccd, v2
	v_lshlrev_b32_e32 v2, 1, v216
	v_lshl_add_u64 v[68:69], s[8:9], 0, v[2:3]
	v_mul_f32_e32 v2, v56, v112
	v_ashrrev_i32_e32 v71, 31, v70
	s_waitcnt vmcnt(3)
	v_mul_f32_e32 v2, v2, v83
	v_lshlrev_b64 v[70:71], 12, v[70:71]
	v_bfe_u32 v56, v2, 16, 1
	v_lshl_add_u64 v[70:71], v[68:69], 0, v[70:71]
	v_add3_u32 v2, v2, v56, s4
	global_store_short_d16_hi v[70:71], v2, off offset:2048
	v_mul_f32_e32 v2, v57, v112
	s_waitcnt vmcnt(3)
	v_mul_f32_e32 v2, v2, v87
	v_bfe_u32 v56, v2, 16, 1
	v_add3_u32 v2, v2, v56, s4
	global_store_short_d16_hi v[70:71], v2, off offset:2112
	v_mul_f32_e32 v2, v66, v112
	s_waitcnt vmcnt(3)
	v_mul_f32_e32 v2, v2, v90
	v_bfe_u32 v56, v2, 16, 1
	v_add3_u32 v2, v2, v56, s4
	global_store_short_d16_hi v[70:71], v2, off offset:2176
	v_mul_f32_e32 v2, v67, v112
	s_waitcnt vmcnt(3)
	v_mul_f32_e32 v2, v2, v91
	v_bfe_u32 v56, v2, 16, 1
	v_add3_u32 v2, v2, v56, s4
	global_store_short_d16_hi v[70:71], v2, off offset:2240
	v_or_b32_e32 v56, s0, v128
	v_mul_f32_e32 v2, v52, v102
	v_ashrrev_i32_e32 v57, 31, v56
	v_mul_f32_e32 v2, v2, v83
	v_lshlrev_b64 v[56:57], 12, v[56:57]
	v_bfe_u32 v52, v2, 16, 1
	v_lshl_add_u64 v[56:57], v[68:69], 0, v[56:57]
	v_add3_u32 v2, v2, v52, s4
	global_store_short_d16_hi v[56:57], v2, off offset:2048
	v_mul_f32_e32 v2, v53, v102
	v_mul_f32_e32 v2, v2, v87
	v_bfe_u32 v52, v2, 16, 1
	v_add3_u32 v2, v2, v52, s4
	global_store_short_d16_hi v[56:57], v2, off offset:2112
	v_mul_f32_e32 v2, v64, v102
	v_mul_f32_e32 v2, v2, v90
	v_bfe_u32 v52, v2, 16, 1
	v_add3_u32 v2, v2, v52, s4
	global_store_short_d16_hi v[56:57], v2, off offset:2176
	v_mul_f32_e32 v2, v65, v102
	v_mul_f32_e32 v2, v2, v91
	v_bfe_u32 v52, v2, 16, 1
	v_add3_u32 v2, v2, v52, s4
	global_store_short_d16_hi v[56:57], v2, off offset:2240
	v_or_b32_e32 v52, s0, v127
	v_mul_f32_e32 v2, v46, v103
	v_ashrrev_i32_e32 v53, 31, v52
	v_mul_f32_e32 v2, v2, v83
	v_lshlrev_b64 v[52:53], 12, v[52:53]
	v_bfe_u32 v46, v2, 16, 1
	v_lshl_add_u64 v[52:53], v[68:69], 0, v[52:53]
	v_add3_u32 v2, v2, v46, s4
	global_store_short_d16_hi v[52:53], v2, off offset:2048
	v_mul_f32_e32 v2, v47, v103
	v_mul_f32_e32 v2, v2, v87
	v_bfe_u32 v46, v2, 16, 1
	v_add3_u32 v2, v2, v46, s4
	global_store_short_d16_hi v[52:53], v2, off offset:2112
	v_mul_f32_e32 v2, v62, v103
	v_mul_f32_e32 v2, v2, v90
	v_bfe_u32 v46, v2, 16, 1
	v_add3_u32 v2, v2, v46, s4
	global_store_short_d16_hi v[52:53], v2, off offset:2176
	v_mul_f32_e32 v2, v63, v103
	v_mul_f32_e32 v2, v2, v91
	v_bfe_u32 v46, v2, 16, 1
	v_add3_u32 v2, v2, v46, s4
	global_store_short_d16_hi v[52:53], v2, off offset:2240
	v_or_b32_e32 v46, s0, v126
	v_mul_f32_e32 v2, v40, v110
	v_ashrrev_i32_e32 v47, 31, v46
	v_mul_f32_e32 v2, v2, v83
	v_lshlrev_b64 v[46:47], 12, v[46:47]
	v_bfe_u32 v40, v2, 16, 1
	v_lshl_add_u64 v[46:47], v[68:69], 0, v[46:47]
	v_add3_u32 v2, v2, v40, s4
	global_store_short_d16_hi v[46:47], v2, off offset:2048
	v_mul_f32_e32 v2, v41, v110
	v_mul_f32_e32 v2, v2, v87
	v_bfe_u32 v40, v2, 16, 1
	v_add3_u32 v2, v2, v40, s4
	global_store_short_d16_hi v[46:47], v2, off offset:2112
	v_mul_f32_e32 v2, v60, v110
	v_mul_f32_e32 v2, v2, v90
	v_bfe_u32 v40, v2, 16, 1
	v_add3_u32 v2, v2, v40, s4
	global_store_short_d16_hi v[46:47], v2, off offset:2176
	v_mul_f32_e32 v2, v61, v110
	v_mul_f32_e32 v2, v2, v91
	v_bfe_u32 v40, v2, 16, 1
	v_add3_u32 v2, v2, v40, s4
	global_store_short_d16_hi v[46:47], v2, off offset:2240
	v_or_b32_e32 v40, s0, v125
	v_mul_f32_e32 v2, v36, v113
	v_ashrrev_i32_e32 v41, 31, v40
	v_mul_f32_e32 v2, v2, v83
	v_lshlrev_b64 v[40:41], 12, v[40:41]
	v_bfe_u32 v36, v2, 16, 1
	v_lshl_add_u64 v[40:41], v[68:69], 0, v[40:41]
	v_add3_u32 v2, v2, v36, s4
	global_store_short_d16_hi v[40:41], v2, off offset:2048
	v_mul_f32_e32 v2, v37, v113
	v_mul_f32_e32 v2, v2, v87
	v_bfe_u32 v36, v2, 16, 1
	v_add3_u32 v2, v2, v36, s4
	global_store_short_d16_hi v[40:41], v2, off offset:2112
	v_mul_f32_e32 v2, v58, v113
	v_mul_f32_e32 v2, v2, v90
	v_bfe_u32 v36, v2, 16, 1
	v_add3_u32 v2, v2, v36, s4
	global_store_short_d16_hi v[40:41], v2, off offset:2176
	v_mul_f32_e32 v2, v59, v113
	v_mul_f32_e32 v2, v2, v91
	v_bfe_u32 v36, v2, 16, 1
	v_mul_f32_e32 v104, 0x3f4ccccd, v104
	v_add3_u32 v2, v2, v36, s4
	global_store_short_d16_hi v[40:41], v2, off offset:2240
	v_or_b32_e32 v36, s0, v124
	v_mul_f32_e32 v2, v32, v104
	v_ashrrev_i32_e32 v37, 31, v36
	v_mul_f32_e32 v2, v2, v83
	v_lshlrev_b64 v[36:37], 12, v[36:37]
	v_bfe_u32 v32, v2, 16, 1
	v_lshl_add_u64 v[36:37], v[68:69], 0, v[36:37]
	v_add3_u32 v2, v2, v32, s4
	global_store_short_d16_hi v[36:37], v2, off offset:2048
	v_mul_f32_e32 v2, v33, v104
	v_mul_f32_e32 v2, v2, v87
	v_bfe_u32 v32, v2, 16, 1
	v_add3_u32 v2, v2, v32, s4
	global_store_short_d16_hi v[36:37], v2, off offset:2112
	v_mul_f32_e32 v2, v54, v104
	v_mul_f32_e32 v2, v2, v90
	v_bfe_u32 v32, v2, 16, 1
	v_add3_u32 v2, v2, v32, s4
	global_store_short_d16_hi v[36:37], v2, off offset:2176
	v_mul_f32_e32 v2, v55, v104
	v_mul_f32_e32 v2, v2, v91
	v_bfe_u32 v32, v2, 16, 1
	v_add3_u32 v2, v2, v32, s4
	global_store_short_d16_hi v[36:37], v2, off offset:2240
	v_or_b32_e32 v32, s0, v123
	v_mul_f32_e32 v2, v28, v97
	v_ashrrev_i32_e32 v33, 31, v32
	v_mul_f32_e32 v2, v2, v83
	v_lshlrev_b64 v[32:33], 12, v[32:33]
	v_bfe_u32 v28, v2, 16, 1
	v_lshl_add_u64 v[32:33], v[68:69], 0, v[32:33]
	v_add3_u32 v2, v2, v28, s4
	global_store_short_d16_hi v[32:33], v2, off offset:2048
	v_mul_f32_e32 v2, v29, v97
	v_mul_f32_e32 v2, v2, v87
	v_bfe_u32 v28, v2, 16, 1
	v_add3_u32 v2, v2, v28, s4
	global_store_short_d16_hi v[32:33], v2, off offset:2112
	v_mul_f32_e32 v2, v48, v97
	v_mul_f32_e32 v2, v2, v90
	v_bfe_u32 v28, v2, 16, 1
	v_add3_u32 v2, v2, v28, s4
	global_store_short_d16_hi v[32:33], v2, off offset:2176
	v_mul_f32_e32 v2, v49, v97
	v_mul_f32_e32 v2, v2, v91
	v_bfe_u32 v28, v2, 16, 1
	v_mul_f32_e32 v94, 0x3f4ccccd, v94
	v_add3_u32 v2, v2, v28, s4
	global_store_short_d16_hi v[32:33], v2, off offset:2240
	v_or_b32_e32 v28, s0, v122
	v_mul_f32_e32 v2, v24, v94
	v_ashrrev_i32_e32 v29, 31, v28
	v_mul_f32_e32 v2, v2, v83
	v_lshlrev_b64 v[28:29], 12, v[28:29]
	v_bfe_u32 v24, v2, 16, 1
	v_lshl_add_u64 v[28:29], v[68:69], 0, v[28:29]
	v_add3_u32 v2, v2, v24, s4
	global_store_short_d16_hi v[28:29], v2, off offset:2048
	v_mul_f32_e32 v2, v25, v94
	v_mul_f32_e32 v2, v2, v87
	v_bfe_u32 v24, v2, 16, 1
	v_add3_u32 v2, v2, v24, s4
	global_store_short_d16_hi v[28:29], v2, off offset:2112
	v_mul_f32_e32 v2, v42, v94
	v_mul_f32_e32 v2, v2, v90
	v_bfe_u32 v24, v2, 16, 1
	v_add3_u32 v2, v2, v24, s4
	global_store_short_d16_hi v[28:29], v2, off offset:2176
	v_mul_f32_e32 v2, v43, v94
	v_mul_f32_e32 v2, v2, v91
	v_bfe_u32 v24, v2, 16, 1
	v_add3_u32 v2, v2, v24, s4
	global_store_short_d16_hi v[28:29], v2, off offset:2240
	v_or_b32_e32 v24, s0, v121
	v_mul_f32_e32 v2, v20, v89
	v_ashrrev_i32_e32 v25, 31, v24
	v_mul_f32_e32 v2, v2, v83
	v_lshlrev_b64 v[24:25], 12, v[24:25]
	v_bfe_u32 v20, v2, 16, 1
	v_lshl_add_u64 v[24:25], v[68:69], 0, v[24:25]
	v_add3_u32 v2, v2, v20, s4
	global_store_short_d16_hi v[24:25], v2, off offset:2048
	v_mul_f32_e32 v2, v21, v89
	v_mul_f32_e32 v2, v2, v87
	v_bfe_u32 v20, v2, 16, 1
	v_add3_u32 v2, v2, v20, s4
	global_store_short_d16_hi v[24:25], v2, off offset:2112
	v_mul_f32_e32 v2, v50, v89
	v_mul_f32_e32 v2, v2, v90
	v_bfe_u32 v20, v2, 16, 1
	v_add3_u32 v2, v2, v20, s4
	global_store_short_d16_hi v[24:25], v2, off offset:2176
	v_mul_f32_e32 v2, v51, v89
	v_mul_f32_e32 v2, v2, v91
	v_bfe_u32 v20, v2, 16, 1
	v_mul_f32_e32 v86, 0x3f4ccccd, v86
	v_add3_u32 v2, v2, v20, s4
	global_store_short_d16_hi v[24:25], v2, off offset:2240
	v_or_b32_e32 v20, s0, v120
	v_mul_f32_e32 v2, v16, v86
	v_ashrrev_i32_e32 v21, 31, v20
	v_mul_f32_e32 v2, v2, v83
	v_lshlrev_b64 v[20:21], 12, v[20:21]
	v_bfe_u32 v16, v2, 16, 1
	v_lshl_add_u64 v[20:21], v[68:69], 0, v[20:21]
	v_add3_u32 v2, v2, v16, s4
	global_store_short_d16_hi v[20:21], v2, off offset:2048
	v_mul_f32_e32 v2, v17, v86
	v_mul_f32_e32 v2, v2, v87
	v_bfe_u32 v16, v2, 16, 1
	v_add3_u32 v2, v2, v16, s4
	global_store_short_d16_hi v[20:21], v2, off offset:2112
	v_mul_f32_e32 v2, v44, v86
	v_mul_f32_e32 v2, v2, v90
	v_bfe_u32 v16, v2, 16, 1
	v_add3_u32 v2, v2, v16, s4
	global_store_short_d16_hi v[20:21], v2, off offset:2176
	v_mul_f32_e32 v2, v45, v86
	v_mul_f32_e32 v2, v2, v91
	v_bfe_u32 v16, v2, 16, 1
	v_mul_f32_e32 v76, 0x3f4ccccd, v82
	v_add3_u32 v2, v2, v16, s4
	global_store_short_d16_hi v[20:21], v2, off offset:2240
	v_or_b32_e32 v16, s0, v119
	v_mul_f32_e32 v2, v14, v76
	v_ashrrev_i32_e32 v17, 31, v16
	v_mul_f32_e32 v2, v2, v83
	v_lshlrev_b64 v[16:17], 12, v[16:17]
	v_bfe_u32 v14, v2, 16, 1
	v_lshl_add_u64 v[16:17], v[68:69], 0, v[16:17]
	v_add3_u32 v2, v2, v14, s4
	global_store_short_d16_hi v[16:17], v2, off offset:2048
	v_mul_f32_e32 v2, v15, v76
	v_mul_f32_e32 v2, v2, v87
	v_bfe_u32 v14, v2, 16, 1
	v_add3_u32 v2, v2, v14, s4
	global_store_short_d16_hi v[16:17], v2, off offset:2112
	v_mul_f32_e32 v2, v38, v76
	v_mul_f32_e32 v2, v2, v90
	v_bfe_u32 v14, v2, 16, 1
	v_add3_u32 v2, v2, v14, s4
	global_store_short_d16_hi v[16:17], v2, off offset:2176
	v_mul_f32_e32 v2, v39, v76
	v_mul_f32_e32 v2, v2, v91
	v_bfe_u32 v14, v2, 16, 1
	v_add3_u32 v2, v2, v14, s4
	global_store_short_d16_hi v[16:17], v2, off offset:2240
	v_or_b32_e32 v14, s0, v118
	v_mul_f32_e32 v2, v12, v74
	v_ashrrev_i32_e32 v15, 31, v14
	v_mul_f32_e32 v2, v2, v83
	v_lshlrev_b64 v[14:15], 12, v[14:15]
	v_bfe_u32 v12, v2, 16, 1
	v_lshl_add_u64 v[14:15], v[68:69], 0, v[14:15]
	v_add3_u32 v2, v2, v12, s4
	global_store_short_d16_hi v[14:15], v2, off offset:2048
	v_mul_f32_e32 v2, v13, v74
	v_mul_f32_e32 v2, v2, v87
	v_bfe_u32 v12, v2, 16, 1
	v_add3_u32 v2, v2, v12, s4
	global_store_short_d16_hi v[14:15], v2, off offset:2112
	v_mul_f32_e32 v2, v34, v74
	v_mul_f32_e32 v2, v2, v90
	v_bfe_u32 v12, v2, 16, 1
	v_add3_u32 v2, v2, v12, s4
	global_store_short_d16_hi v[14:15], v2, off offset:2176
	v_mul_f32_e32 v2, v35, v74
	v_mul_f32_e32 v2, v2, v91
	v_bfe_u32 v12, v2, 16, 1
	v_add3_u32 v2, v2, v12, s4
	global_store_short_d16_hi v[14:15], v2, off offset:2240
	v_or_b32_e32 v12, s0, v117
	v_mul_f32_e32 v2, v10, v73
	v_ashrrev_i32_e32 v13, 31, v12
	v_mul_f32_e32 v2, v2, v83
	v_lshlrev_b64 v[12:13], 12, v[12:13]
	v_bfe_u32 v10, v2, 16, 1
	v_lshl_add_u64 v[12:13], v[68:69], 0, v[12:13]
	v_add3_u32 v2, v2, v10, s4
	global_store_short_d16_hi v[12:13], v2, off offset:2048
	v_mul_f32_e32 v2, v11, v73
	v_mul_f32_e32 v2, v2, v87
	v_bfe_u32 v10, v2, 16, 1
	v_add3_u32 v2, v2, v10, s4
	global_store_short_d16_hi v[12:13], v2, off offset:2112
	v_mul_f32_e32 v2, v30, v73
	v_mul_f32_e32 v2, v2, v90
	v_bfe_u32 v10, v2, 16, 1
	v_add3_u32 v2, v2, v10, s4
	global_store_short_d16_hi v[12:13], v2, off offset:2176
	v_mul_f32_e32 v2, v31, v73
	v_mul_f32_e32 v2, v2, v91
	v_bfe_u32 v10, v2, 16, 1
	v_add3_u32 v2, v2, v10, s4
	global_store_short_d16_hi v[12:13], v2, off offset:2240
	v_or_b32_e32 v10, s0, v116
	v_mul_f32_e32 v2, v8, v72
	v_ashrrev_i32_e32 v11, 31, v10
	v_mul_f32_e32 v2, v2, v83
	v_lshlrev_b64 v[10:11], 12, v[10:11]
	v_bfe_u32 v8, v2, 16, 1
	v_lshl_add_u64 v[10:11], v[68:69], 0, v[10:11]
	v_add3_u32 v2, v2, v8, s4
	global_store_short_d16_hi v[10:11], v2, off offset:2048
	v_mul_f32_e32 v2, v9, v72
	v_mul_f32_e32 v2, v2, v87
	v_bfe_u32 v8, v2, 16, 1
	v_add3_u32 v2, v2, v8, s4
	global_store_short_d16_hi v[10:11], v2, off offset:2112
	v_mul_f32_e32 v2, v26, v72
	v_mul_f32_e32 v2, v2, v90
	v_bfe_u32 v8, v2, 16, 1
	v_add3_u32 v2, v2, v8, s4
	global_store_short_d16_hi v[10:11], v2, off offset:2176
	v_mul_f32_e32 v2, v27, v72
	v_mul_f32_e32 v2, v2, v91
	v_bfe_u32 v8, v2, 16, 1
	v_add3_u32 v2, v2, v8, s4
	global_store_short_d16_hi v[10:11], v2, off offset:2240
	v_or_b32_e32 v8, s0, v115
	v_mul_f32_e32 v2, v6, v75
	v_ashrrev_i32_e32 v9, 31, v8
	v_mul_f32_e32 v2, v83, v2
	v_lshlrev_b64 v[8:9], 12, v[8:9]
	v_bfe_u32 v6, v2, 16, 1
	v_lshl_add_u64 v[8:9], v[68:69], 0, v[8:9]
	v_add3_u32 v2, v2, v6, s4
	global_store_short_d16_hi v[8:9], v2, off offset:2048
	v_mul_f32_e32 v2, v7, v75
	v_mul_f32_e32 v2, v87, v2
	v_bfe_u32 v6, v2, 16, 1
	v_add3_u32 v2, v2, v6, s4
	global_store_short_d16_hi v[8:9], v2, off offset:2112
	v_mul_f32_e32 v2, v22, v75
	v_mul_f32_e32 v2, v90, v2
	v_bfe_u32 v6, v2, 16, 1
	v_add3_u32 v2, v2, v6, s4
	global_store_short_d16_hi v[8:9], v2, off offset:2176
	v_mul_f32_e32 v2, v23, v75
	v_mul_f32_e32 v2, v91, v2
	v_bfe_u32 v6, v2, 16, 1
	v_add3_u32 v2, v2, v6, s4
	global_store_short_d16_hi v[8:9], v2, off offset:2240
	v_or_b32_e32 v6, s0, v114
	v_mul_f32_e32 v2, v4, v77
	v_ashrrev_i32_e32 v7, 31, v6
	v_mul_f32_e32 v2, v83, v2
	v_lshlrev_b64 v[6:7], 12, v[6:7]
	v_bfe_u32 v4, v2, 16, 1
	v_lshl_add_u64 v[6:7], v[68:69], 0, v[6:7]
	v_add3_u32 v2, v2, v4, s4
	global_store_short_d16_hi v[6:7], v2, off offset:2048
	v_mul_f32_e32 v2, v5, v77
	v_mul_f32_e32 v2, v87, v2
	v_bfe_u32 v4, v2, 16, 1
	v_add3_u32 v2, v2, v4, s4
	global_store_short_d16_hi v[6:7], v2, off offset:2112
	v_mul_f32_e32 v2, v18, v77
	v_mul_f32_e32 v2, v90, v2
	v_bfe_u32 v4, v2, 16, 1
	v_add3_u32 v2, v2, v4, s4
	global_store_short_d16_hi v[6:7], v2, off offset:2176
	v_mul_f32_e32 v2, v19, v77
	v_mul_f32_e32 v2, v91, v2
	v_bfe_u32 v4, v2, 16, 1
	v_add3_u32 v2, v2, v4, s4
	global_store_short_d16_hi v[6:7], v2, off offset:2240
	s_branch .LBB0_409
